# MoBA/SWA attention units: unit-end wait before the LDS barrier reduced from vmcnt(0) lgkmcnt(0) to lgkmcnt(0) (O-store acks drain into the next unit)
# baseline (speedup 1.0000x reference)
.LBB0_515:
	s_or_b64 exec, exec, s[0:1]
	s_waitcnt lgkmcnt(0)
	ds_read_b32 v32, v168 offset:49152
	v_add_u32_e32 v33, v169, v170
	s_lshl_b32 s0, s29, 10
	v_readlane_b32 s1, v254, 48
	s_add_u32 s0, s1, s0
	s_waitcnt lgkmcnt(0)
	v_mul_f32_e32 v0, v0, v32
	v_cvt_pk_bf16_f32 v0, v0, v117
	ds_write_b16 v33, v0 offset:51200
	v_mul_f32_e32 v0, v16, v32
	v_cvt_pk_bf16_f32 v0, v0, v117
	ds_write_b16 v33, v0 offset:51264
	ds_read_b32 v0, v168 offset:49156
	v_readlane_b32 s1, v254, 49
	s_addc_u32 s1, s1, 0
	s_add_u32 s0, s0, s31
	s_addc_u32 s1, s1, 0
	s_waitcnt lgkmcnt(0)
	v_mul_f32_e32 v1, v1, v0
	v_mul_f32_e32 v0, v17, v0
	v_cvt_pk_bf16_f32 v1, v1, v117
	ds_write_b16 v172, v1 offset:51200
	v_cvt_pk_bf16_f32 v0, v0, v117
	ds_write_b16 v172, v0 offset:51264
	ds_read_b32 v0, v168 offset:49160
	s_lshl_b64 s[6:7], s[8:9], 10
	s_add_u32 s0, s0, s6
	s_addc_u32 s1, s1, s7
	s_waitcnt lgkmcnt(0)
	v_mul_f32_e32 v1, v2, v0
	v_mul_f32_e32 v0, v18, v0
	v_cvt_pk_bf16_f32 v1, v1, v117
	ds_write_b16 v173, v1 offset:51200
	v_cvt_pk_bf16_f32 v0, v0, v117
	ds_write_b16 v173, v0 offset:51264
	ds_read_b32 v0, v168 offset:49164
	s_waitcnt lgkmcnt(0)
	v_mul_f32_e32 v1, v3, v0
	v_mul_f32_e32 v0, v19, v0
	v_cvt_pk_bf16_f32 v1, v1, v117
	ds_write_b16 v174, v1 offset:51200
	v_cvt_pk_bf16_f32 v0, v0, v117
	ds_write_b16 v174, v0 offset:51264
	ds_read_b32 v0, v168 offset:49184
	s_waitcnt lgkmcnt(0)
	v_mul_f32_e32 v1, v4, v0
	v_mul_f32_e32 v0, v20, v0
	v_cvt_pk_bf16_f32 v1, v1, v117
	ds_write_b16 v175, v1 offset:51200
	v_cvt_pk_bf16_f32 v0, v0, v117
	ds_write_b16 v175, v0 offset:51264
	ds_read_b32 v0, v168 offset:49188
	s_waitcnt lgkmcnt(0)
	v_mul_f32_e32 v1, v5, v0
	v_mul_f32_e32 v0, v21, v0
	v_cvt_pk_bf16_f32 v1, v1, v117
	ds_write_b16 v176, v1 offset:51200
	v_cvt_pk_bf16_f32 v0, v0, v117
	ds_write_b16 v176, v0 offset:51264
	ds_read_b32 v0, v168 offset:49192
	s_waitcnt lgkmcnt(0)
	v_mul_f32_e32 v1, v6, v0
	v_mul_f32_e32 v0, v22, v0
	v_cvt_pk_bf16_f32 v1, v1, v117
	ds_write_b16 v177, v1 offset:51200
	v_cvt_pk_bf16_f32 v0, v0, v117
	ds_write_b16 v177, v0 offset:51264
	ds_read_b32 v0, v168 offset:49196
	s_waitcnt lgkmcnt(0)
	v_mul_f32_e32 v1, v7, v0
	v_mul_f32_e32 v0, v23, v0
	v_cvt_pk_bf16_f32 v1, v1, v117
	ds_write_b16 v178, v1 offset:51200
	v_cvt_pk_bf16_f32 v0, v0, v117
	ds_write_b16 v178, v0 offset:51264
	ds_read_b32 v0, v168 offset:49216
	s_waitcnt lgkmcnt(0)
	v_mul_f32_e32 v1, v8, v0
	v_mul_f32_e32 v0, v24, v0
	v_cvt_pk_bf16_f32 v1, v1, v117
	ds_write_b16 v179, v1 offset:51200
	v_cvt_pk_bf16_f32 v0, v0, v117
	ds_write_b16 v179, v0 offset:51264
	ds_read_b32 v0, v168 offset:49220
	s_waitcnt lgkmcnt(0)
	v_mul_f32_e32 v1, v9, v0
	v_mul_f32_e32 v0, v25, v0
	v_cvt_pk_bf16_f32 v1, v1, v117
	ds_write_b16 v180, v1 offset:51200
	v_cvt_pk_bf16_f32 v0, v0, v117
	ds_write_b16 v180, v0 offset:51264
	ds_read_b32 v0, v168 offset:49224
	s_waitcnt lgkmcnt(0)
	v_mul_f32_e32 v1, v10, v0
	v_mul_f32_e32 v0, v26, v0
	v_cvt_pk_bf16_f32 v1, v1, v117
	ds_write_b16 v181, v1 offset:51200
	v_cvt_pk_bf16_f32 v0, v0, v117
	ds_write_b16 v181, v0 offset:51264
	ds_read_b32 v0, v168 offset:49228
	s_waitcnt lgkmcnt(0)
	v_mul_f32_e32 v1, v11, v0
	v_mul_f32_e32 v0, v27, v0
	v_cvt_pk_bf16_f32 v1, v1, v117
	ds_write_b16 v182, v1 offset:51200
	v_cvt_pk_bf16_f32 v0, v0, v117
	ds_write_b16 v182, v0 offset:51264
	ds_read_b32 v0, v168 offset:49248
	s_waitcnt lgkmcnt(0)
	v_mul_f32_e32 v1, v12, v0
	v_mul_f32_e32 v0, v28, v0
	v_cvt_pk_bf16_f32 v1, v1, v117
	ds_write_b16 v183, v1 offset:51200
	v_cvt_pk_bf16_f32 v0, v0, v117
	ds_write_b16 v183, v0 offset:51264
	ds_read_b32 v0, v168 offset:49252
	s_waitcnt lgkmcnt(0)
	v_mul_f32_e32 v1, v13, v0
	v_mul_f32_e32 v0, v29, v0
	v_cvt_pk_bf16_f32 v1, v1, v117
	ds_write_b16 v184, v1 offset:51200
	v_cvt_pk_bf16_f32 v0, v0, v117
	ds_write_b16 v184, v0 offset:51264
	ds_read_b32 v0, v168 offset:49256
	s_waitcnt lgkmcnt(0)
	v_mul_f32_e32 v1, v14, v0
	v_mul_f32_e32 v0, v30, v0
	v_cvt_pk_bf16_f32 v1, v1, v117
	ds_write_b16 v185, v1 offset:51200
	v_cvt_pk_bf16_f32 v0, v0, v117
	ds_write_b16 v185, v0 offset:51264
	ds_read_b32 v0, v168 offset:49260
	s_waitcnt lgkmcnt(0)
	v_mul_f32_e32 v1, v15, v0
	v_mul_f32_e32 v0, v31, v0
	v_cvt_pk_bf16_f32 v1, v1, v117
	ds_write_b16 v186, v1 offset:51200
	v_cvt_pk_bf16_f32 v0, v0, v117
	ds_write_b16 v186, v0 offset:51264
	s_waitcnt lgkmcnt(0)
	ds_read_b128 v[2:5], v187 offset:51200
	v_lshl_add_u64 v[0:1], s[0:1], 0, v[122:123]
	s_waitcnt lgkmcnt(0)
	v_lshlrev_b32_e32 v6, 16, v2
	v_and_b32_e32 v2, 0xffff0000, v2
	v_lshlrev_b32_e32 v8, 16, v4
	v_and_b32_e32 v4, 0xffff0000, v4
	v_mul_f32_e32 v2, 0x41800000, v2
	v_lshlrev_b32_e32 v7, 16, v3
	v_med3_f32 v10, v2, s28, v193
	v_mul_f32_e32 v2, 0x41800000, v4
	v_lshlrev_b32_e32 v9, 16, v5
	v_med3_f32 v4, v2, s28, v193
	v_mul_f32_e32 v2, 0x41800000, v7
	v_and_b32_e32 v3, 0xffff0000, v3
	v_med3_f32 v7, v2, s28, v193
	v_mul_f32_e32 v2, 0x41800000, v9
	v_and_b32_e32 v5, 0xffff0000, v5
	v_med3_f32 v9, v2, s28, v193
	v_mul_f32_e32 v2, 0x41800000, v3
	v_mul_f32_e32 v6, 0x41800000, v6
	v_med3_f32 v3, v2, s28, v193
	v_mul_f32_e32 v2, 0x41800000, v5
	v_med3_f32 v6, v6, s28, v193
	v_med3_f32 v5, v2, s28, v193
	v_mov_b32_e32 v2, 0
	v_cvt_pk_fp8_f32 v2, v6, v10
	v_mul_f32_e32 v8, 0x41800000, v8
	v_med3_f32 v8, v8, s28, v193
	v_cvt_pk_fp8_f32 v2, v7, v3 op_sel:[0,0,1]
	v_mov_b32_e32 v3, 0
	v_cvt_pk_fp8_f32 v3, v8, v4
	v_cvt_pk_fp8_f32 v3, v9, v5 op_sel:[0,0,1]
	v_lshl_add_u64 v[4:5], v[0:1], 0, v[124:125]
	global_store_dwordx2 v[4:5], v[2:3], off
	ds_read_b128 v[2:5], v188 offset:51200
	s_waitcnt lgkmcnt(0)
	v_lshlrev_b32_e32 v6, 16, v2
	v_and_b32_e32 v2, 0xffff0000, v2
	v_lshlrev_b32_e32 v8, 16, v4
	v_and_b32_e32 v4, 0xffff0000, v4
	v_mul_f32_e32 v2, 0x41800000, v2
	v_lshlrev_b32_e32 v7, 16, v3
	v_med3_f32 v10, v2, s28, v193
	v_mul_f32_e32 v2, 0x41800000, v4
	v_lshlrev_b32_e32 v9, 16, v5
	v_med3_f32 v4, v2, s28, v193
	v_mul_f32_e32 v2, 0x41800000, v7
	v_and_b32_e32 v3, 0xffff0000, v3
	v_med3_f32 v7, v2, s28, v193
	v_mul_f32_e32 v2, 0x41800000, v9
	v_and_b32_e32 v5, 0xffff0000, v5
	v_med3_f32 v9, v2, s28, v193
	v_mul_f32_e32 v2, 0x41800000, v3
	v_mul_f32_e32 v6, 0x41800000, v6
	v_med3_f32 v3, v2, s28, v193
	v_mul_f32_e32 v2, 0x41800000, v5
	v_med3_f32 v6, v6, s28, v193
	v_med3_f32 v5, v2, s28, v193
	v_mov_b32_e32 v2, 0
	v_cvt_pk_fp8_f32 v2, v6, v10
	v_mul_f32_e32 v8, 0x41800000, v8
	v_med3_f32 v8, v8, s28, v193
	v_cvt_pk_fp8_f32 v2, v7, v3 op_sel:[0,0,1]
	v_mov_b32_e32 v3, 0
	v_cvt_pk_fp8_f32 v3, v8, v4
	v_cvt_pk_fp8_f32 v3, v9, v5 op_sel:[0,0,1]
	v_lshl_add_u64 v[4:5], v[0:1], 0, v[126:127]
	global_store_dwordx2 v[4:5], v[2:3], off
	ds_read_b128 v[2:5], v189 offset:51200
	s_waitcnt lgkmcnt(0)
	v_lshlrev_b32_e32 v6, 16, v2
	v_and_b32_e32 v2, 0xffff0000, v2
	v_lshlrev_b32_e32 v8, 16, v4
	v_and_b32_e32 v4, 0xffff0000, v4
	v_mul_f32_e32 v2, 0x41800000, v2
	v_lshlrev_b32_e32 v7, 16, v3
	v_med3_f32 v10, v2, s28, v193
	v_mul_f32_e32 v2, 0x41800000, v4
	v_lshlrev_b32_e32 v9, 16, v5
	v_med3_f32 v4, v2, s28, v193
	v_mul_f32_e32 v2, 0x41800000, v7
	v_and_b32_e32 v3, 0xffff0000, v3
	v_med3_f32 v7, v2, s28, v193
	v_mul_f32_e32 v2, 0x41800000, v9
	v_and_b32_e32 v5, 0xffff0000, v5
	v_med3_f32 v9, v2, s28, v193
	v_mul_f32_e32 v2, 0x41800000, v3
	v_mul_f32_e32 v6, 0x41800000, v6
	v_med3_f32 v3, v2, s28, v193
	v_mul_f32_e32 v2, 0x41800000, v5
	v_med3_f32 v6, v6, s28, v193
	v_med3_f32 v5, v2, s28, v193
	v_mov_b32_e32 v2, 0
	v_cvt_pk_fp8_f32 v2, v6, v10
	v_mul_f32_e32 v8, 0x41800000, v8
	v_med3_f32 v8, v8, s28, v193
	v_cvt_pk_fp8_f32 v2, v7, v3 op_sel:[0,0,1]
	v_mov_b32_e32 v3, 0
	v_cvt_pk_fp8_f32 v3, v8, v4
	v_cvt_pk_fp8_f32 v3, v9, v5 op_sel:[0,0,1]
	v_lshl_add_u64 v[4:5], v[0:1], 0, v[128:129]
	v_lshl_add_u64 v[0:1], v[0:1], 0, v[130:131]
	global_store_dwordx2 v[4:5], v[2:3], off
	ds_read_b128 v[2:5], v190 offset:51200
	s_waitcnt lgkmcnt(0)
	v_lshlrev_b32_e32 v6, 16, v2
	v_and_b32_e32 v2, 0xffff0000, v2
	v_lshlrev_b32_e32 v8, 16, v4
	v_and_b32_e32 v4, 0xffff0000, v4
	v_mul_f32_e32 v2, 0x41800000, v2
	v_lshlrev_b32_e32 v7, 16, v3
	v_med3_f32 v10, v2, s28, v193
	v_mul_f32_e32 v2, 0x41800000, v4
	v_lshlrev_b32_e32 v9, 16, v5
	v_med3_f32 v4, v2, s28, v193
	v_mul_f32_e32 v2, 0x41800000, v7
	v_and_b32_e32 v3, 0xffff0000, v3
	v_med3_f32 v7, v2, s28, v193
	v_mul_f32_e32 v2, 0x41800000, v9
	v_and_b32_e32 v5, 0xffff0000, v5
	v_med3_f32 v9, v2, s28, v193
	v_mul_f32_e32 v2, 0x41800000, v3
	v_mul_f32_e32 v6, 0x41800000, v6
	v_med3_f32 v3, v2, s28, v193
	v_mul_f32_e32 v2, 0x41800000, v5
	v_med3_f32 v6, v6, s28, v193
	v_med3_f32 v5, v2, s28, v193
	v_mov_b32_e32 v2, 0
	v_cvt_pk_fp8_f32 v2, v6, v10
	v_mul_f32_e32 v8, 0x41800000, v8
	v_med3_f32 v8, v8, s28, v193
	v_cvt_pk_fp8_f32 v2, v7, v3 op_sel:[0,0,1]
	v_mov_b32_e32 v3, 0
	v_cvt_pk_fp8_f32 v3, v8, v4
	v_cvt_pk_fp8_f32 v3, v9, v5 op_sel:[0,0,1]
	global_store_dwordx2 v[0:1], v[2:3], off
	s_waitcnt lgkmcnt(0)
	s_barrier
	s_and_saveexec_b64 s[0:1], s[2:3]
	s_cbranch_execz .LBB0_465
	v_mov_b32_e32 v0, s16
	ds_write_b32 v0, v194
	s_branch .LBB0_465

.LBB0_1427:
	s_or_b64 exec, exec, s[38:39]
	s_waitcnt lgkmcnt(0)
	ds_read_b32 v32, v160 offset:49152
	v_add_u32_e32 v33, v161, v162
	s_lshl_b32 s38, s40, 10
	v_readlane_b32 s39, v254, 48
	s_add_u32 s38, s39, s38
	s_waitcnt lgkmcnt(0)
	v_mul_f32_e32 v0, v0, v32
	v_cvt_pk_bf16_f32 v0, v0, v117
	ds_write_b16 v33, v0 offset:51200
	v_mul_f32_e32 v0, v16, v32
	v_cvt_pk_bf16_f32 v0, v0, v117
	ds_write_b16 v33, v0 offset:51264
	ds_read_b32 v0, v160 offset:49156
	v_readlane_b32 s39, v254, 49
	s_addc_u32 s39, s39, 0
	s_add_u32 s38, s38, s41
	s_addc_u32 s39, s39, 0
	s_waitcnt lgkmcnt(0)
	v_mul_f32_e32 v1, v1, v0
	v_mul_f32_e32 v0, v17, v0
	v_cvt_pk_bf16_f32 v1, v1, v117
	ds_write_b16 v165, v1 offset:51200
	v_cvt_pk_bf16_f32 v0, v0, v117
	ds_write_b16 v165, v0 offset:51264
	ds_read_b32 v0, v160 offset:49160
	s_lshl_b64 s[40:41], s[0:1], 10
	s_add_u32 s38, s38, s40
	s_addc_u32 s39, s39, s41
	s_waitcnt lgkmcnt(0)
	v_mul_f32_e32 v1, v2, v0
	v_mul_f32_e32 v0, v18, v0
	v_cvt_pk_bf16_f32 v1, v1, v117
	ds_write_b16 v166, v1 offset:51200
	v_cvt_pk_bf16_f32 v0, v0, v117
	ds_write_b16 v166, v0 offset:51264
	ds_read_b32 v0, v160 offset:49164
	s_waitcnt lgkmcnt(0)
	v_mul_f32_e32 v1, v3, v0
	v_mul_f32_e32 v0, v19, v0
	v_cvt_pk_bf16_f32 v1, v1, v117
	ds_write_b16 v167, v1 offset:51200
	v_cvt_pk_bf16_f32 v0, v0, v117
	ds_write_b16 v167, v0 offset:51264
	ds_read_b32 v0, v160 offset:49184
	s_waitcnt lgkmcnt(0)
	v_mul_f32_e32 v1, v4, v0
	v_mul_f32_e32 v0, v20, v0
	v_cvt_pk_bf16_f32 v1, v1, v117
	ds_write_b16 v168, v1 offset:51200
	v_cvt_pk_bf16_f32 v0, v0, v117
	ds_write_b16 v168, v0 offset:51264
	ds_read_b32 v0, v160 offset:49188
	s_waitcnt lgkmcnt(0)
	v_mul_f32_e32 v1, v5, v0
	v_mul_f32_e32 v0, v21, v0
	v_cvt_pk_bf16_f32 v1, v1, v117
	ds_write_b16 v169, v1 offset:51200
	v_cvt_pk_bf16_f32 v0, v0, v117
	ds_write_b16 v169, v0 offset:51264
	ds_read_b32 v0, v160 offset:49192
	s_waitcnt lgkmcnt(0)
	v_mul_f32_e32 v1, v6, v0
	v_mul_f32_e32 v0, v22, v0
	v_cvt_pk_bf16_f32 v1, v1, v117
	ds_write_b16 v170, v1 offset:51200
	v_cvt_pk_bf16_f32 v0, v0, v117
	ds_write_b16 v170, v0 offset:51264
	ds_read_b32 v0, v160 offset:49196
	s_waitcnt lgkmcnt(0)
	v_mul_f32_e32 v1, v7, v0
	v_mul_f32_e32 v0, v23, v0
	v_cvt_pk_bf16_f32 v1, v1, v117
	ds_write_b16 v171, v1 offset:51200
	v_cvt_pk_bf16_f32 v0, v0, v117
	ds_write_b16 v171, v0 offset:51264
	ds_read_b32 v0, v160 offset:49216
	s_waitcnt lgkmcnt(0)
	v_mul_f32_e32 v1, v8, v0
	v_mul_f32_e32 v0, v24, v0
	v_cvt_pk_bf16_f32 v1, v1, v117
	ds_write_b16 v172, v1 offset:51200
	v_cvt_pk_bf16_f32 v0, v0, v117
	ds_write_b16 v172, v0 offset:51264
	ds_read_b32 v0, v160 offset:49220
	s_waitcnt lgkmcnt(0)
	v_mul_f32_e32 v1, v9, v0
	v_mul_f32_e32 v0, v25, v0
	v_cvt_pk_bf16_f32 v1, v1, v117
	ds_write_b16 v173, v1 offset:51200
	v_cvt_pk_bf16_f32 v0, v0, v117
	ds_write_b16 v173, v0 offset:51264
	ds_read_b32 v0, v160 offset:49224
	s_waitcnt lgkmcnt(0)
	v_mul_f32_e32 v1, v10, v0
	v_mul_f32_e32 v0, v26, v0
	v_cvt_pk_bf16_f32 v1, v1, v117
	ds_write_b16 v174, v1 offset:51200
	v_cvt_pk_bf16_f32 v0, v0, v117
	ds_write_b16 v174, v0 offset:51264
	ds_read_b32 v0, v160 offset:49228
	s_waitcnt lgkmcnt(0)
	v_mul_f32_e32 v1, v11, v0
	v_mul_f32_e32 v0, v27, v0
	v_cvt_pk_bf16_f32 v1, v1, v117
	ds_write_b16 v175, v1 offset:51200
	v_cvt_pk_bf16_f32 v0, v0, v117
	ds_write_b16 v175, v0 offset:51264
	ds_read_b32 v0, v160 offset:49248
	s_waitcnt lgkmcnt(0)
	v_mul_f32_e32 v1, v12, v0
	v_mul_f32_e32 v0, v28, v0
	v_cvt_pk_bf16_f32 v1, v1, v117
	ds_write_b16 v176, v1 offset:51200
	v_cvt_pk_bf16_f32 v0, v0, v117
	ds_write_b16 v176, v0 offset:51264
	ds_read_b32 v0, v160 offset:49252
	s_waitcnt lgkmcnt(0)
	v_mul_f32_e32 v1, v13, v0
	v_mul_f32_e32 v0, v29, v0
	v_cvt_pk_bf16_f32 v1, v1, v117
	ds_write_b16 v177, v1 offset:51200
	v_cvt_pk_bf16_f32 v0, v0, v117
	ds_write_b16 v177, v0 offset:51264
	ds_read_b32 v0, v160 offset:49256
	s_waitcnt lgkmcnt(0)
	v_mul_f32_e32 v1, v14, v0
	v_mul_f32_e32 v0, v30, v0
	v_cvt_pk_bf16_f32 v1, v1, v117
	ds_write_b16 v178, v1 offset:51200
	v_cvt_pk_bf16_f32 v0, v0, v117
	ds_write_b16 v178, v0 offset:51264
	ds_read_b32 v0, v160 offset:49260
	s_waitcnt lgkmcnt(0)
	v_mul_f32_e32 v1, v15, v0
	v_mul_f32_e32 v0, v31, v0
	v_cvt_pk_bf16_f32 v1, v1, v117
	ds_write_b16 v179, v1 offset:51200
	v_cvt_pk_bf16_f32 v0, v0, v117
	ds_write_b16 v179, v0 offset:51264
	s_waitcnt lgkmcnt(0)
	ds_read_b128 v[2:5], v180 offset:51200
	v_lshl_add_u64 v[0:1], s[38:39], 0, v[120:121]
	s_waitcnt lgkmcnt(0)
	v_lshlrev_b32_e32 v6, 16, v2
	v_and_b32_e32 v2, 0xffff0000, v2
	v_lshlrev_b32_e32 v8, 16, v4
	v_and_b32_e32 v4, 0xffff0000, v4
	v_mul_f32_e32 v2, 0x41800000, v2
	v_lshlrev_b32_e32 v7, 16, v3
	v_med3_f32 v10, v2, s33, v187
	v_mul_f32_e32 v2, 0x41800000, v4
	v_lshlrev_b32_e32 v9, 16, v5
	v_med3_f32 v4, v2, s33, v187
	v_mul_f32_e32 v2, 0x41800000, v7
	v_and_b32_e32 v3, 0xffff0000, v3
	v_med3_f32 v7, v2, s33, v187
	v_mul_f32_e32 v2, 0x41800000, v9
	v_and_b32_e32 v5, 0xffff0000, v5
	v_med3_f32 v9, v2, s33, v187
	v_mul_f32_e32 v2, 0x41800000, v3
	v_mul_f32_e32 v6, 0x41800000, v6
	v_med3_f32 v3, v2, s33, v187
	v_mul_f32_e32 v2, 0x41800000, v5
	v_med3_f32 v6, v6, s33, v187
	v_med3_f32 v5, v2, s33, v187
	v_mov_b32_e32 v2, 0
	v_cvt_pk_fp8_f32 v2, v6, v10
	v_mul_f32_e32 v8, 0x41800000, v8
	v_med3_f32 v8, v8, s33, v187
	v_cvt_pk_fp8_f32 v2, v7, v3 op_sel:[0,0,1]
	v_mov_b32_e32 v3, 0
	v_cvt_pk_fp8_f32 v3, v8, v4
	v_cvt_pk_fp8_f32 v3, v9, v5 op_sel:[0,0,1]
	v_lshl_add_u64 v[4:5], v[0:1], 0, v[122:123]
	global_store_dwordx2 v[4:5], v[2:3], off
	ds_read_b128 v[2:5], v181 offset:51200
	s_waitcnt lgkmcnt(0)
	v_lshlrev_b32_e32 v6, 16, v2
	v_and_b32_e32 v2, 0xffff0000, v2
	v_lshlrev_b32_e32 v8, 16, v4
	v_and_b32_e32 v4, 0xffff0000, v4
	v_mul_f32_e32 v2, 0x41800000, v2
	v_lshlrev_b32_e32 v7, 16, v3
	v_med3_f32 v10, v2, s33, v187
	v_mul_f32_e32 v2, 0x41800000, v4
	v_lshlrev_b32_e32 v9, 16, v5
	v_med3_f32 v4, v2, s33, v187
	v_mul_f32_e32 v2, 0x41800000, v7
	v_and_b32_e32 v3, 0xffff0000, v3
	v_med3_f32 v7, v2, s33, v187
	v_mul_f32_e32 v2, 0x41800000, v9
	v_and_b32_e32 v5, 0xffff0000, v5
	v_med3_f32 v9, v2, s33, v187
	v_mul_f32_e32 v2, 0x41800000, v3
	v_mul_f32_e32 v6, 0x41800000, v6
	v_med3_f32 v3, v2, s33, v187
	v_mul_f32_e32 v2, 0x41800000, v5
	v_med3_f32 v6, v6, s33, v187
	v_med3_f32 v5, v2, s33, v187
	v_mov_b32_e32 v2, 0
	v_cvt_pk_fp8_f32 v2, v6, v10
	v_mul_f32_e32 v8, 0x41800000, v8
	v_med3_f32 v8, v8, s33, v187
	v_cvt_pk_fp8_f32 v2, v7, v3 op_sel:[0,0,1]
	v_mov_b32_e32 v3, 0
	v_cvt_pk_fp8_f32 v3, v8, v4
	v_cvt_pk_fp8_f32 v3, v9, v5 op_sel:[0,0,1]
	v_lshl_add_u64 v[4:5], v[0:1], 0, v[124:125]
	global_store_dwordx2 v[4:5], v[2:3], off
	ds_read_b128 v[2:5], v182 offset:51200
	s_waitcnt lgkmcnt(0)
	v_lshlrev_b32_e32 v6, 16, v2
	v_and_b32_e32 v2, 0xffff0000, v2
	v_lshlrev_b32_e32 v8, 16, v4
	v_and_b32_e32 v4, 0xffff0000, v4
	v_mul_f32_e32 v2, 0x41800000, v2
	v_lshlrev_b32_e32 v7, 16, v3
	v_med3_f32 v10, v2, s33, v187
	v_mul_f32_e32 v2, 0x41800000, v4
	v_lshlrev_b32_e32 v9, 16, v5
	v_med3_f32 v4, v2, s33, v187
	v_mul_f32_e32 v2, 0x41800000, v7
	v_and_b32_e32 v3, 0xffff0000, v3
	v_med3_f32 v7, v2, s33, v187
	v_mul_f32_e32 v2, 0x41800000, v9
	v_and_b32_e32 v5, 0xffff0000, v5
	v_med3_f32 v9, v2, s33, v187
	v_mul_f32_e32 v2, 0x41800000, v3
	v_mul_f32_e32 v6, 0x41800000, v6
	v_med3_f32 v3, v2, s33, v187
	v_mul_f32_e32 v2, 0x41800000, v5
	v_med3_f32 v6, v6, s33, v187
	v_med3_f32 v5, v2, s33, v187
	v_mov_b32_e32 v2, 0
	v_cvt_pk_fp8_f32 v2, v6, v10
	v_mul_f32_e32 v8, 0x41800000, v8
	v_med3_f32 v8, v8, s33, v187
	v_cvt_pk_fp8_f32 v2, v7, v3 op_sel:[0,0,1]
	v_mov_b32_e32 v3, 0
	v_cvt_pk_fp8_f32 v3, v8, v4
	v_cvt_pk_fp8_f32 v3, v9, v5 op_sel:[0,0,1]
	v_lshl_add_u64 v[4:5], v[0:1], 0, v[126:127]
	v_lshl_add_u64 v[0:1], v[0:1], 0, v[128:129]
	global_store_dwordx2 v[4:5], v[2:3], off
	ds_read_b128 v[2:5], v183 offset:51200
	s_waitcnt lgkmcnt(0)
	v_lshlrev_b32_e32 v6, 16, v2
	v_and_b32_e32 v2, 0xffff0000, v2
	v_lshlrev_b32_e32 v8, 16, v4
	v_and_b32_e32 v4, 0xffff0000, v4
	v_mul_f32_e32 v2, 0x41800000, v2
	v_lshlrev_b32_e32 v7, 16, v3
	v_med3_f32 v10, v2, s33, v187
	v_mul_f32_e32 v2, 0x41800000, v4
	v_lshlrev_b32_e32 v9, 16, v5
	v_med3_f32 v4, v2, s33, v187
	v_mul_f32_e32 v2, 0x41800000, v7
	v_and_b32_e32 v3, 0xffff0000, v3
	v_med3_f32 v7, v2, s33, v187
	v_mul_f32_e32 v2, 0x41800000, v9
	v_and_b32_e32 v5, 0xffff0000, v5
	v_med3_f32 v9, v2, s33, v187
	v_mul_f32_e32 v2, 0x41800000, v3
	v_mul_f32_e32 v6, 0x41800000, v6
	v_med3_f32 v3, v2, s33, v187
	v_mul_f32_e32 v2, 0x41800000, v5
	v_med3_f32 v6, v6, s33, v187
	v_med3_f32 v5, v2, s33, v187
	v_mov_b32_e32 v2, 0
	v_cvt_pk_fp8_f32 v2, v6, v10
	v_mul_f32_e32 v8, 0x41800000, v8
	v_med3_f32 v8, v8, s33, v187
	v_cvt_pk_fp8_f32 v2, v7, v3 op_sel:[0,0,1]
	v_mov_b32_e32 v3, 0
	v_cvt_pk_fp8_f32 v3, v8, v4
	v_cvt_pk_fp8_f32 v3, v9, v5 op_sel:[0,0,1]
	global_store_dwordx2 v[0:1], v[2:3], off
	s_waitcnt lgkmcnt(0)
	s_barrier
	s_and_saveexec_b64 s[38:39], s[2:3]
	s_cbranch_execz .LBB0_1400
	v_mov_b32_e32 v0, s18
	ds_write_b32 v0, v188
	s_branch .LBB0_1400

.LBB0_3054:
	s_or_b64 exec, exec, s[0:1]
	s_waitcnt lgkmcnt(0)
	ds_read_b32 v32, v168 offset:49152
	v_add_u32_e32 v33, v169, v170
	s_lshl_b32 s0, s50, 10
	v_readlane_b32 s1, v254, 48
	s_add_u32 s0, s1, s0
	s_waitcnt lgkmcnt(0)
	v_mul_f32_e32 v0, v0, v32
	v_mul_f32_e32 v16, v16, v32
	v_cvt_pk_bf16_f32 v0, v0, v117
	ds_write_b16 v33, v0 offset:51200
	v_cvt_pk_bf16_f32 v0, v16, v117
	ds_read_b32 v16, v168 offset:49156
	ds_write_b16 v33, v0 offset:51264
	v_readlane_b32 s1, v254, 49
	s_addc_u32 s1, s1, 0
	s_add_u32 s6, s0, s51
	s_waitcnt lgkmcnt(0)
	v_mul_f32_e32 v0, v1, v16
	v_mul_f32_e32 v1, v17, v16
	v_cvt_pk_bf16_f32 v0, v0, v117
	ds_write_b16 v172, v0 offset:51200
	v_cvt_pk_bf16_f32 v0, v1, v117
	ds_read_b32 v1, v168 offset:49160
	ds_write_b16 v172, v0 offset:51264
	s_addc_u32 s7, s1, 0
	s_lshl_b64 s[0:1], s[8:9], 10
	s_add_u32 s0, s6, s0
	s_waitcnt lgkmcnt(0)
	v_mul_f32_e32 v0, v2, v1
	v_mul_f32_e32 v1, v18, v1
	v_cvt_pk_bf16_f32 v0, v0, v117
	ds_write_b16 v173, v0 offset:51200
	v_cvt_pk_bf16_f32 v0, v1, v117
	ds_read_b32 v1, v168 offset:49164
	ds_write_b16 v173, v0 offset:51264
	s_addc_u32 s1, s7, s1
	s_waitcnt lgkmcnt(0)
	v_mul_f32_e32 v0, v3, v1
	v_mul_f32_e32 v1, v19, v1
	v_cvt_pk_bf16_f32 v0, v0, v117
	ds_write_b16 v174, v0 offset:51200
	v_cvt_pk_bf16_f32 v0, v1, v117
	ds_read_b32 v1, v168 offset:49184
	ds_write_b16 v174, v0 offset:51264
	s_waitcnt lgkmcnt(0)
	v_mul_f32_e32 v0, v4, v1
	v_mul_f32_e32 v1, v20, v1
	v_cvt_pk_bf16_f32 v0, v0, v117
	ds_write_b16 v175, v0 offset:51200
	v_cvt_pk_bf16_f32 v0, v1, v117
	ds_read_b32 v1, v168 offset:49188
	ds_write_b16 v175, v0 offset:51264
	s_waitcnt lgkmcnt(0)
	v_mul_f32_e32 v0, v5, v1
	v_mul_f32_e32 v1, v21, v1
	v_cvt_pk_bf16_f32 v0, v0, v117
	ds_write_b16 v176, v0 offset:51200
	v_cvt_pk_bf16_f32 v0, v1, v117
	ds_read_b32 v1, v168 offset:49192
	ds_write_b16 v176, v0 offset:51264
	s_waitcnt lgkmcnt(0)
	v_mul_f32_e32 v0, v6, v1
	v_mul_f32_e32 v1, v22, v1
	v_cvt_pk_bf16_f32 v0, v0, v117
	ds_write_b16 v177, v0 offset:51200
	v_cvt_pk_bf16_f32 v0, v1, v117
	ds_read_b32 v1, v168 offset:49196
	ds_write_b16 v177, v0 offset:51264
	s_waitcnt lgkmcnt(0)
	v_mul_f32_e32 v0, v7, v1
	v_mul_f32_e32 v1, v23, v1
	v_cvt_pk_bf16_f32 v0, v0, v117
	ds_write_b16 v178, v0 offset:51200
	v_cvt_pk_bf16_f32 v0, v1, v117
	ds_read_b32 v1, v168 offset:49216
	ds_write_b16 v178, v0 offset:51264
	s_waitcnt lgkmcnt(0)
	v_mul_f32_e32 v0, v8, v1
	v_mul_f32_e32 v1, v24, v1
	v_cvt_pk_bf16_f32 v0, v0, v117
	ds_write_b16 v179, v0 offset:51200
	v_cvt_pk_bf16_f32 v0, v1, v117
	ds_read_b32 v1, v168 offset:49220
	ds_write_b16 v179, v0 offset:51264
	s_waitcnt lgkmcnt(0)
	v_mul_f32_e32 v0, v9, v1
	v_mul_f32_e32 v1, v25, v1
	v_cvt_pk_bf16_f32 v0, v0, v117
	ds_write_b16 v180, v0 offset:51200
	v_cvt_pk_bf16_f32 v0, v1, v117
	ds_read_b32 v1, v168 offset:49224
	ds_write_b16 v180, v0 offset:51264
	v_lshl_add_u64 v[8:9], s[0:1], 0, v[122:123]
	s_waitcnt lgkmcnt(0)
	v_mul_f32_e32 v0, v10, v1
	v_mul_f32_e32 v1, v26, v1
	v_cvt_pk_bf16_f32 v0, v0, v117
	ds_write_b16 v181, v0 offset:51200
	v_cvt_pk_bf16_f32 v0, v1, v117
	ds_read_b32 v1, v168 offset:49228
	ds_write_b16 v181, v0 offset:51264
	s_waitcnt lgkmcnt(0)
	v_mul_f32_e32 v0, v11, v1
	v_mul_f32_e32 v1, v27, v1
	v_cvt_pk_bf16_f32 v0, v0, v117
	ds_write_b16 v182, v0 offset:51200
	v_cvt_pk_bf16_f32 v0, v1, v117
	ds_read_b32 v1, v168 offset:49248
	ds_write_b16 v182, v0 offset:51264
	s_waitcnt lgkmcnt(0)
	v_mul_f32_e32 v0, v12, v1
	v_mul_f32_e32 v1, v28, v1
	v_cvt_pk_bf16_f32 v0, v0, v117
	ds_write_b16 v183, v0 offset:51200
	v_cvt_pk_bf16_f32 v0, v1, v117
	ds_read_b32 v1, v168 offset:49252
	ds_write_b16 v183, v0 offset:51264
	s_waitcnt lgkmcnt(0)
	v_mul_f32_e32 v0, v13, v1
	v_mul_f32_e32 v1, v29, v1
	v_cvt_pk_bf16_f32 v0, v0, v117
	ds_write_b16 v184, v0 offset:51200
	v_cvt_pk_bf16_f32 v0, v1, v117
	ds_read_b32 v1, v168 offset:49256
	ds_write_b16 v184, v0 offset:51264
	s_waitcnt lgkmcnt(0)
	v_mul_f32_e32 v0, v14, v1
	v_mul_f32_e32 v1, v30, v1
	v_cvt_pk_bf16_f32 v0, v0, v117
	ds_write_b16 v185, v0 offset:51200
	v_cvt_pk_bf16_f32 v0, v1, v117
	ds_read_b32 v1, v168 offset:49260
	ds_write_b16 v185, v0 offset:51264
	s_waitcnt lgkmcnt(0)
	v_mul_f32_e32 v0, v15, v1
	v_cvt_pk_bf16_f32 v0, v0, v117
	ds_write_b16 v186, v0 offset:51200
	v_mul_f32_e32 v0, v31, v1
	v_cvt_pk_bf16_f32 v0, v0, v117
	ds_write_b16 v186, v0 offset:51264
	s_waitcnt lgkmcnt(0)
	ds_read_b128 v[0:3], v187 offset:51200
	ds_read_b128 v[4:7], v188 offset:51200
	s_waitcnt lgkmcnt(0)
	v_lshlrev_b32_e32 v10, 16, v0
	v_lshlrev_b32_e32 v12, 16, v2
	v_mul_f32_e32 v10, 0x41800000, v10
	v_lshlrev_b32_e32 v11, 16, v1
	v_med3_f32 v14, v10, s49, v193
	v_mul_f32_e32 v10, 0x41800000, v12
	v_and_b32_e32 v0, 0xffff0000, v0
	v_and_b32_e32 v2, 0xffff0000, v2
	v_lshlrev_b32_e32 v13, 16, v3
	v_med3_f32 v12, v10, s49, v193
	v_mul_f32_e32 v10, 0x41800000, v11
	v_mul_f32_e32 v0, 0x41800000, v0
	v_mul_f32_e32 v2, 0x41800000, v2
	v_med3_f32 v15, v10, s49, v193
	v_mul_f32_e32 v10, 0x41800000, v13
	v_med3_f32 v0, v0, s49, v193
	v_med3_f32 v2, v2, s49, v193
	v_med3_f32 v13, v10, s49, v193
	v_mov_b32_e32 v10, 0
	v_mov_b32_e32 v11, 0
	v_cvt_pk_fp8_f32 v10, v14, v0
	v_cvt_pk_fp8_f32 v11, v12, v2
	v_and_b32_e32 v1, 0xffff0000, v1
	v_and_b32_e32 v3, 0xffff0000, v3
	v_mul_f32_e32 v1, 0x41800000, v1
	v_mul_f32_e32 v0, 0x41800000, v3
	v_med3_f32 v1, v1, s49, v193
	v_med3_f32 v0, v0, s49, v193
	v_cvt_pk_fp8_f32 v10, v15, v1 op_sel:[0,0,1]
	v_cvt_pk_fp8_f32 v11, v13, v0 op_sel:[0,0,1]
	v_lshlrev_b32_e32 v0, 16, v4
	v_and_b32_e32 v1, 0xffff0000, v4
	v_lshlrev_b32_e32 v4, 16, v6
	v_lshlrev_b32_e32 v2, 16, v5
	v_and_b32_e32 v3, 0xffff0000, v5
	v_and_b32_e32 v5, 0xffff0000, v6
	v_mul_f32_e32 v4, 0x41800000, v4
	v_lshlrev_b32_e32 v6, 16, v7
	v_med3_f32 v14, v4, s49, v193
	v_mul_f32_e32 v4, 0x41800000, v5
	v_mul_f32_e32 v0, 0x41800000, v0
	v_mul_f32_e32 v1, 0x41800000, v1
	v_med3_f32 v15, v4, s49, v193
	v_mul_f32_e32 v4, 0x41800000, v6
	v_med3_f32 v0, v0, s49, v193
	v_med3_f32 v1, v1, s49, v193
	v_med3_f32 v6, v4, s49, v193
	v_mov_b32_e32 v4, 0
	v_mov_b32_e32 v5, 0
	v_cvt_pk_fp8_f32 v4, v0, v1
	v_cvt_pk_fp8_f32 v5, v14, v15
	v_and_b32_e32 v7, 0xffff0000, v7
	v_mul_f32_e32 v2, 0x41800000, v2
	v_mul_f32_e32 v3, 0x41800000, v3
	v_mul_f32_e32 v0, 0x41800000, v7
	v_med3_f32 v2, v2, s49, v193
	v_med3_f32 v3, v3, s49, v193
	v_med3_f32 v0, v0, s49, v193
	v_cvt_pk_fp8_f32 v4, v2, v3 op_sel:[0,0,1]
	v_cvt_pk_fp8_f32 v5, v6, v0 op_sel:[0,0,1]
	ds_read_b128 v[0:3], v189 offset:51200
	v_lshl_add_u64 v[12:13], v[8:9], 0, v[124:125]
	v_lshl_add_u64 v[6:7], v[8:9], 0, v[126:127]
	global_store_dwordx2 v[12:13], v[10:11], off
	global_store_dwordx2 v[6:7], v[4:5], off
	ds_read_b128 v[4:7], v190 offset:51200
	s_waitcnt lgkmcnt(0)
	v_lshlrev_b32_e32 v10, 16, v0
	v_and_b32_e32 v0, 0xffff0000, v0
	v_lshlrev_b32_e32 v12, 16, v2
	v_and_b32_e32 v2, 0xffff0000, v2
	v_mul_f32_e32 v0, 0x41800000, v0
	v_lshlrev_b32_e32 v11, 16, v1
	v_med3_f32 v14, v0, s49, v193
	v_mul_f32_e32 v0, 0x41800000, v2
	v_lshlrev_b32_e32 v13, 16, v3
	v_med3_f32 v2, v0, s49, v193
	v_mul_f32_e32 v0, 0x41800000, v11
	v_and_b32_e32 v1, 0xffff0000, v1
	v_mul_f32_e32 v12, 0x41800000, v12
	v_med3_f32 v11, v0, s49, v193
	v_mul_f32_e32 v0, 0x41800000, v13
	v_med3_f32 v12, v12, s49, v193
	v_med3_f32 v13, v0, s49, v193
	v_mul_f32_e32 v0, 0x41800000, v1
	v_mov_b32_e32 v1, 0
	v_cvt_pk_fp8_f32 v1, v12, v2
	v_and_b32_e32 v3, 0xffff0000, v3
	v_mul_f32_e32 v2, 0x41800000, v3
	v_mul_f32_e32 v10, 0x41800000, v10
	v_med3_f32 v2, v2, s49, v193
	v_med3_f32 v10, v10, s49, v193
	v_med3_f32 v15, v0, s49, v193
	v_mov_b32_e32 v0, 0
	v_cvt_pk_fp8_f32 v1, v13, v2 op_sel:[0,0,1]
	v_lshlrev_b32_e32 v2, 16, v4
	v_cvt_pk_fp8_f32 v0, v10, v14
	v_lshlrev_b32_e32 v10, 16, v6
	v_mul_f32_e32 v2, 0x41800000, v2
	v_and_b32_e32 v3, 0xffff0000, v4
	v_med3_f32 v12, v2, s49, v193
	v_mul_f32_e32 v2, 0x41800000, v10
	v_and_b32_e32 v6, 0xffff0000, v6
	v_med3_f32 v10, v2, s49, v193
	v_mul_f32_e32 v2, 0x41800000, v3
	v_lshlrev_b32_e32 v4, 16, v5
	v_med3_f32 v3, v2, s49, v193
	v_mul_f32_e32 v2, 0x41800000, v6
	v_cvt_pk_fp8_f32 v0, v11, v15 op_sel:[0,0,1]
	v_lshlrev_b32_e32 v11, 16, v7
	v_med3_f32 v6, v2, s49, v193
	v_mul_f32_e32 v2, 0x41800000, v4
	v_and_b32_e32 v5, 0xffff0000, v5
	v_med3_f32 v4, v2, s49, v193
	v_mul_f32_e32 v2, 0x41800000, v11
	v_med3_f32 v11, v2, s49, v193
	v_mul_f32_e32 v2, 0x41800000, v5
	v_med3_f32 v5, v2, s49, v193
	v_mov_b32_e32 v2, 0
	v_cvt_pk_fp8_f32 v2, v12, v3
	v_mov_b32_e32 v3, 0
	v_cvt_pk_fp8_f32 v3, v10, v6
	v_and_b32_e32 v7, 0xffff0000, v7
	v_mul_f32_e32 v6, 0x41800000, v7
	v_med3_f32 v6, v6, s49, v193
	v_cvt_pk_fp8_f32 v2, v4, v5 op_sel:[0,0,1]
	v_cvt_pk_fp8_f32 v3, v11, v6 op_sel:[0,0,1]
	v_lshl_add_u64 v[4:5], v[8:9], 0, v[128:129]
	global_store_dwordx2 v[4:5], v[0:1], off
	v_lshl_add_u64 v[0:1], v[8:9], 0, v[130:131]
	global_store_dwordx2 v[0:1], v[2:3], off
	s_waitcnt lgkmcnt(0)
	s_barrier
	s_and_saveexec_b64 s[0:1], s[2:3]
	s_cbranch_execz .LBB0_3004
	v_mov_b32_e32 v0, s33
	ds_write_b32 v0, v194
	s_branch .LBB0_3004
